# differential-attention QK^T fragment reads interleaved behind the MFMAs and running two slices ahead (sets in unused VGPRs), slices 0-1 read during the last P.V block
# speedup vs baseline: 1.0105x; 1.0006x over previous
.LBB0_557:
	ds_read_b64_tr_b16 v[144:145], v177 offset:0
	ds_read_b64_tr_b16 v[146:147], v177 offset:0x1000
	ds_read_b64_tr_b16 v[148:149], v177 offset:0x2000
	ds_read_b64_tr_b16 v[150:151], v177 offset:0x3000
	ds_read_b64_tr_b16 v[152:153], v177 offset:0x4000
	ds_read_b64_tr_b16 v[154:155], v177 offset:0x5000
	ds_read_b64_tr_b16 v[156:157], v177 offset:0x6000
	ds_read_b64_tr_b16 v[158:159], v177 offset:0x7000
	s_waitcnt lgkmcnt(6)
	s_nop 0
	v_mfma_f32_32x32x16_bf16 v[112:127], v[144:147], v[128:131], v[112:127]
	ds_read_b64_tr_b16 v[192:193], v177 offset:0x200
	ds_read_b64_tr_b16 v[194:195], v177 offset:0x1200
	s_waitcnt lgkmcnt(6)
	v_mfma_f32_32x32x16_bf16 v[112:127], v[148:151], v[132:135], v[112:127]
	ds_read_b64_tr_b16 v[196:197], v177 offset:0x2200
	ds_read_b64_tr_b16 v[198:199], v177 offset:0x3200
	s_waitcnt lgkmcnt(6)
	v_mfma_f32_32x32x16_bf16 v[112:127], v[152:155], v[136:139], v[112:127]
	ds_read_b64_tr_b16 v[200:201], v177 offset:0x4200
	ds_read_b64_tr_b16 v[202:203], v177 offset:0x5200
	s_waitcnt lgkmcnt(6)
	v_mfma_f32_32x32x16_bf16 v[112:127], v[156:159], v[140:143], v[112:127]
	ds_read_b64_tr_b16 v[204:205], v177 offset:0x6200
	ds_read_b64_tr_b16 v[206:207], v177 offset:0x7200
	s_waitcnt lgkmcnt(6)
	v_mfma_f32_32x32x16_bf16 v[80:95], v[192:195], v[128:131], v[80:95]
	ds_read_b64_tr_b16 v[144:145], v177 offset:0x400
	ds_read_b64_tr_b16 v[146:147], v177 offset:0x1400
	s_waitcnt lgkmcnt(6)
	v_mfma_f32_32x32x16_bf16 v[80:95], v[196:199], v[132:135], v[80:95]
	ds_read_b64_tr_b16 v[148:149], v177 offset:0x2400
	ds_read_b64_tr_b16 v[150:151], v177 offset:0x3400
	s_waitcnt lgkmcnt(6)
	v_mfma_f32_32x32x16_bf16 v[80:95], v[200:203], v[136:139], v[80:95]
	ds_read_b64_tr_b16 v[152:153], v177 offset:0x4400
	ds_read_b64_tr_b16 v[154:155], v177 offset:0x5400
	s_waitcnt lgkmcnt(6)
	v_mfma_f32_32x32x16_bf16 v[80:95], v[204:207], v[140:143], v[80:95]
	ds_read_b64_tr_b16 v[156:157], v177 offset:0x6400
	ds_read_b64_tr_b16 v[158:159], v177 offset:0x7400
	s_waitcnt lgkmcnt(6)
	v_mfma_f32_32x32x16_bf16 v[96:111], v[144:147], v[128:131], v[96:111]
	ds_read_b64_tr_b16 v[192:193], v177 offset:0x600
	ds_read_b64_tr_b16 v[194:195], v177 offset:0x1600
	s_waitcnt lgkmcnt(6)
	v_mfma_f32_32x32x16_bf16 v[96:111], v[148:151], v[132:135], v[96:111]
	ds_read_b64_tr_b16 v[196:197], v177 offset:0x2600
	ds_read_b64_tr_b16 v[198:199], v177 offset:0x3600
	s_waitcnt lgkmcnt(6)
	v_mfma_f32_32x32x16_bf16 v[96:111], v[152:155], v[136:139], v[96:111]
	ds_read_b64_tr_b16 v[200:201], v177 offset:0x4600
	ds_read_b64_tr_b16 v[202:203], v177 offset:0x5600
	s_waitcnt lgkmcnt(6)
	v_mfma_f32_32x32x16_bf16 v[96:111], v[156:159], v[140:143], v[96:111]
	ds_read_b64_tr_b16 v[204:205], v177 offset:0x6600
	ds_read_b64_tr_b16 v[206:207], v177 offset:0x7600
	s_waitcnt lgkmcnt(6)
	v_mfma_f32_32x32x16_bf16 v[64:79], v[192:195], v[128:131], v[64:79]
	ds_read_b64_tr_b16 v[144:145], v177 offset:0x800
	ds_read_b64_tr_b16 v[146:147], v177 offset:0x1800
	s_waitcnt lgkmcnt(6)
	v_mfma_f32_32x32x16_bf16 v[64:79], v[196:199], v[132:135], v[64:79]
	ds_read_b64_tr_b16 v[148:149], v177 offset:0x2800
	ds_read_b64_tr_b16 v[150:151], v177 offset:0x3800
	s_waitcnt lgkmcnt(6)
	v_mfma_f32_32x32x16_bf16 v[64:79], v[200:203], v[136:139], v[64:79]
	ds_read_b64_tr_b16 v[152:153], v177 offset:0x4800
	ds_read_b64_tr_b16 v[154:155], v177 offset:0x5800
	s_waitcnt lgkmcnt(6)
	v_mfma_f32_32x32x16_bf16 v[64:79], v[204:207], v[140:143], v[64:79]
	ds_read_b64_tr_b16 v[156:157], v177 offset:0x6800
	ds_read_b64_tr_b16 v[158:159], v177 offset:0x7800
	s_waitcnt lgkmcnt(6)
	v_mfma_f32_32x32x16_bf16 v[48:63], v[144:147], v[128:131], v[48:63]
	ds_read_b64_tr_b16 v[192:193], v177 offset:0xa00
	ds_read_b64_tr_b16 v[194:195], v177 offset:0x1a00
	s_waitcnt lgkmcnt(6)
	v_mfma_f32_32x32x16_bf16 v[48:63], v[148:151], v[132:135], v[48:63]
	ds_read_b64_tr_b16 v[196:197], v177 offset:0x2a00
	ds_read_b64_tr_b16 v[198:199], v177 offset:0x3a00
	s_waitcnt lgkmcnt(6)
	v_mfma_f32_32x32x16_bf16 v[48:63], v[152:155], v[136:139], v[48:63]
	ds_read_b64_tr_b16 v[200:201], v177 offset:0x4a00
	ds_read_b64_tr_b16 v[202:203], v177 offset:0x5a00
	s_waitcnt lgkmcnt(6)
	v_mfma_f32_32x32x16_bf16 v[48:63], v[156:159], v[140:143], v[48:63]
	ds_read_b64_tr_b16 v[204:205], v177 offset:0x6a00
	ds_read_b64_tr_b16 v[206:207], v177 offset:0x7a00
	s_waitcnt lgkmcnt(6)
	v_mfma_f32_32x32x16_bf16 v[32:47], v[192:195], v[128:131], v[32:47]
	ds_read_b64_tr_b16 v[144:145], v177 offset:0xc00
	ds_read_b64_tr_b16 v[146:147], v177 offset:0x1c00
	s_waitcnt lgkmcnt(6)
	v_mfma_f32_32x32x16_bf16 v[32:47], v[196:199], v[132:135], v[32:47]
	ds_read_b64_tr_b16 v[148:149], v177 offset:0x2c00
	ds_read_b64_tr_b16 v[150:151], v177 offset:0x3c00
	s_waitcnt lgkmcnt(6)
	v_mfma_f32_32x32x16_bf16 v[32:47], v[200:203], v[136:139], v[32:47]
	ds_read_b64_tr_b16 v[152:153], v177 offset:0x4c00
	ds_read_b64_tr_b16 v[154:155], v177 offset:0x5c00
	s_waitcnt lgkmcnt(6)
	v_mfma_f32_32x32x16_bf16 v[32:47], v[204:207], v[140:143], v[32:47]
	ds_read_b64_tr_b16 v[156:157], v177 offset:0x6c00
	ds_read_b64_tr_b16 v[158:159], v177 offset:0x7c00
	s_waitcnt lgkmcnt(6)
	v_mfma_f32_32x32x16_bf16 v[16:31], v[144:147], v[128:131], v[16:31]
	ds_read_b64_tr_b16 v[192:193], v177 offset:0xe00
	ds_read_b64_tr_b16 v[194:195], v177 offset:0x1e00
	s_waitcnt lgkmcnt(6)
	v_mfma_f32_32x32x16_bf16 v[16:31], v[148:151], v[132:135], v[16:31]
	ds_read_b64_tr_b16 v[196:197], v177 offset:0x2e00
	ds_read_b64_tr_b16 v[198:199], v177 offset:0x3e00
	s_waitcnt lgkmcnt(6)
	v_mfma_f32_32x32x16_bf16 v[16:31], v[152:155], v[136:139], v[16:31]
	ds_read_b64_tr_b16 v[200:201], v177 offset:0x4e00
	ds_read_b64_tr_b16 v[202:203], v177 offset:0x5e00
	s_waitcnt lgkmcnt(6)
	v_mfma_f32_32x32x16_bf16 v[16:31], v[156:159], v[140:143], v[16:31]
	ds_read_b64_tr_b16 v[204:205], v177 offset:0x6e00
	ds_read_b64_tr_b16 v[206:207], v177 offset:0x7e00
	s_waitcnt lgkmcnt(6)
	v_mfma_f32_32x32x16_bf16 v[0:15], v[192:195], v[128:131], v[0:15]
	ds_read_b128 v[236:239], v188 offset:0
	ds_read_b128 v[240:243], v188 offset:0x2000
	s_waitcnt lgkmcnt(6)
	v_mfma_f32_32x32x16_bf16 v[0:15], v[196:199], v[132:135], v[0:15]
	ds_read_b128 v[244:247], v180 offset:0
	ds_read_b128 v[248:251], v187 offset:0
	s_waitcnt lgkmcnt(6)
	v_mfma_f32_32x32x16_bf16 v[0:15], v[200:203], v[136:139], v[0:15]
	ds_read_b128 v[218:221], v187 offset:0x2000
	ds_read_b128 v[222:225], v180 offset:0x400
	s_waitcnt lgkmcnt(6)
	v_mfma_f32_32x32x16_bf16 v[0:15], v[204:207], v[140:143], v[0:15]
	s_waitcnt lgkmcnt(3)
	s_nop 0
	v_mfma_f32_32x32x16_bf16 v[144:159], v[236:239], v[244:247], 0
	ds_read_b128 v[192:195], v186 offset:0
	ds_read_b128 v[196:199], v186 offset:0x2000
	v_mfma_f32_32x32x16_bf16 v[128:143], v[240:243], v[244:247], 0
	ds_read_b128 v[200:203], v180 offset:0x800
	s_waitcnt lgkmcnt(3)
	v_mfma_f32_32x32x16_bf16 v[144:159], v[248:251], v[222:225], v[144:159]
	ds_read_b128 v[236:239], v185 offset:0
	ds_read_b128 v[240:243], v185 offset:0x2000
	v_mfma_f32_32x32x16_bf16 v[128:143], v[218:221], v[222:225], v[128:143]
	ds_read_b128 v[244:247], v180 offset:0xc00
	s_waitcnt lgkmcnt(3)
	v_mfma_f32_32x32x16_bf16 v[144:159], v[192:195], v[200:203], v[144:159]
	ds_read_b128 v[248:251], v188 offset:0x80
	ds_read_b128 v[218:221], v188 offset:0x2080
	v_mfma_f32_32x32x16_bf16 v[128:143], v[196:199], v[200:203], v[128:143]
	ds_read_b128 v[222:225], v180 offset:0x1000
	s_waitcnt lgkmcnt(3)
	v_mfma_f32_32x32x16_bf16 v[144:159], v[236:239], v[244:247], v[144:159]
	ds_read_b128 v[192:195], v187 offset:0x80
	ds_read_b128 v[196:199], v187 offset:0x2080
	v_mfma_f32_32x32x16_bf16 v[128:143], v[240:243], v[244:247], v[128:143]
	ds_read_b128 v[200:203], v180 offset:0x1400
	s_waitcnt lgkmcnt(3)
	v_mfma_f32_32x32x16_bf16 v[144:159], v[248:251], v[222:225], v[144:159]
	ds_read_b128 v[236:239], v186 offset:0x80
	ds_read_b128 v[240:243], v186 offset:0x2080
	v_mfma_f32_32x32x16_bf16 v[128:143], v[218:221], v[222:225], v[128:143]
	ds_read_b128 v[244:247], v180 offset:0x1800
	s_waitcnt lgkmcnt(3)
	v_mfma_f32_32x32x16_bf16 v[144:159], v[192:195], v[200:203], v[144:159]
	ds_read_b128 v[248:251], v185 offset:0x80
	ds_read_b128 v[218:221], v185 offset:0x2080
	v_mfma_f32_32x32x16_bf16 v[128:143], v[196:199], v[200:203], v[128:143]
	s_waitcnt lgkmcnt(2)
	v_mfma_f32_32x32x16_bf16 v[144:159], v[236:239], v[244:247], v[144:159]
	v_mfma_f32_32x32x16_bf16 v[128:143], v[240:243], v[244:247], v[128:143]
	s_waitcnt lgkmcnt(0)
	v_mfma_f32_32x32x16_bf16 v[144:159], v[248:251], v[166:169], v[144:159]
	v_mfma_f32_32x32x16_bf16 v[128:143], v[218:221], v[166:169], v[128:143]
	s_bitcmp0_b32 s100, 8
	s_cbranch_scc1 .Lstg_a10
	s_waitcnt vmcnt(0)
	s_waitcnt lgkmcnt(0)
	s_barrier

.LBB0_565:
	ds_read_b64_tr_b16 v[144:145], v177 offset:0x8000
	ds_read_b64_tr_b16 v[146:147], v177 offset:0x9000
	ds_read_b64_tr_b16 v[148:149], v177 offset:0xa000
	ds_read_b64_tr_b16 v[150:151], v177 offset:0xb000
	ds_read_b64_tr_b16 v[152:153], v177 offset:0xc000
	ds_read_b64_tr_b16 v[154:155], v177 offset:0xd000
	ds_read_b64_tr_b16 v[156:157], v177 offset:0xe000
	ds_read_b64_tr_b16 v[158:159], v177 offset:0xf000
	s_waitcnt lgkmcnt(6)
	s_nop 0
	v_mfma_f32_32x32x16_bf16 v[112:127], v[144:147], v[128:131], v[112:127]
	ds_read_b64_tr_b16 v[194:195], v177 offset:0x8200
	ds_read_b64_tr_b16 v[196:197], v177 offset:0x9200
	s_waitcnt lgkmcnt(6)
	v_mfma_f32_32x32x16_bf16 v[112:127], v[148:151], v[132:135], v[112:127]
	ds_read_b64_tr_b16 v[198:199], v177 offset:0xa200
	ds_read_b64_tr_b16 v[200:201], v177 offset:0xb200
	s_waitcnt lgkmcnt(6)
	v_mfma_f32_32x32x16_bf16 v[112:127], v[152:155], v[136:139], v[112:127]
	ds_read_b64_tr_b16 v[202:203], v177 offset:0xc200
	ds_read_b64_tr_b16 v[204:205], v177 offset:0xd200
	s_waitcnt lgkmcnt(6)
	v_mfma_f32_32x32x16_bf16 v[112:127], v[156:159], v[140:143], v[112:127]
	ds_read_b64_tr_b16 v[206:207], v177 offset:0xe200
	ds_read_b64_tr_b16 v[208:209], v177 offset:0xf200
	s_waitcnt lgkmcnt(6)
	v_mfma_f32_32x32x16_bf16 v[80:95], v[194:197], v[128:131], v[80:95]
	ds_read_b64_tr_b16 v[144:145], v177 offset:0x8400
	ds_read_b64_tr_b16 v[146:147], v177 offset:0x9400
	s_waitcnt lgkmcnt(6)
	v_mfma_f32_32x32x16_bf16 v[80:95], v[198:201], v[132:135], v[80:95]
	ds_read_b64_tr_b16 v[148:149], v177 offset:0xa400
	ds_read_b64_tr_b16 v[150:151], v177 offset:0xb400
	s_waitcnt lgkmcnt(6)
	v_mfma_f32_32x32x16_bf16 v[80:95], v[202:205], v[136:139], v[80:95]
	ds_read_b64_tr_b16 v[152:153], v177 offset:0xc400
	ds_read_b64_tr_b16 v[154:155], v177 offset:0xd400
	s_waitcnt lgkmcnt(6)
	v_mfma_f32_32x32x16_bf16 v[80:95], v[206:209], v[140:143], v[80:95]
	ds_read_b64_tr_b16 v[156:157], v177 offset:0xe400
	ds_read_b64_tr_b16 v[158:159], v177 offset:0xf400
	s_waitcnt lgkmcnt(6)
	v_mfma_f32_32x32x16_bf16 v[96:111], v[144:147], v[128:131], v[96:111]
	ds_read_b64_tr_b16 v[194:195], v177 offset:0x8600
	ds_read_b64_tr_b16 v[196:197], v177 offset:0x9600
	s_waitcnt lgkmcnt(6)
	v_mfma_f32_32x32x16_bf16 v[96:111], v[148:151], v[132:135], v[96:111]
	ds_read_b64_tr_b16 v[198:199], v177 offset:0xa600
	ds_read_b64_tr_b16 v[200:201], v177 offset:0xb600
	s_waitcnt lgkmcnt(6)
	v_mfma_f32_32x32x16_bf16 v[96:111], v[152:155], v[136:139], v[96:111]
	ds_read_b64_tr_b16 v[202:203], v177 offset:0xc600
	ds_read_b64_tr_b16 v[204:205], v177 offset:0xd600
	s_waitcnt lgkmcnt(6)
	v_mfma_f32_32x32x16_bf16 v[96:111], v[156:159], v[140:143], v[96:111]
	ds_read_b64_tr_b16 v[206:207], v177 offset:0xe600
	ds_read_b64_tr_b16 v[208:209], v177 offset:0xf600
	s_waitcnt lgkmcnt(6)
	v_mfma_f32_32x32x16_bf16 v[64:79], v[194:197], v[128:131], v[64:79]
	ds_read_b64_tr_b16 v[144:145], v177 offset:0x8800
	ds_read_b64_tr_b16 v[146:147], v177 offset:0x9800
	s_waitcnt lgkmcnt(6)
	v_mfma_f32_32x32x16_bf16 v[64:79], v[198:201], v[132:135], v[64:79]
	ds_read_b64_tr_b16 v[148:149], v177 offset:0xa800
	ds_read_b64_tr_b16 v[150:151], v177 offset:0xb800
	s_waitcnt lgkmcnt(6)
	v_mfma_f32_32x32x16_bf16 v[64:79], v[202:205], v[136:139], v[64:79]
	ds_read_b64_tr_b16 v[152:153], v177 offset:0xc800
	ds_read_b64_tr_b16 v[154:155], v177 offset:0xd800
	s_waitcnt lgkmcnt(6)
	v_mfma_f32_32x32x16_bf16 v[64:79], v[206:209], v[140:143], v[64:79]
	ds_read_b64_tr_b16 v[156:157], v177 offset:0xe800
	ds_read_b64_tr_b16 v[158:159], v177 offset:0xf800
	s_waitcnt lgkmcnt(6)
	v_mfma_f32_32x32x16_bf16 v[48:63], v[144:147], v[128:131], v[48:63]
	ds_read_b64_tr_b16 v[194:195], v177 offset:0x8a00
	ds_read_b64_tr_b16 v[196:197], v177 offset:0x9a00
	s_waitcnt lgkmcnt(6)
	v_mfma_f32_32x32x16_bf16 v[48:63], v[148:151], v[132:135], v[48:63]
	ds_read_b64_tr_b16 v[198:199], v177 offset:0xaa00
	ds_read_b64_tr_b16 v[200:201], v177 offset:0xba00
	s_waitcnt lgkmcnt(6)
	v_mfma_f32_32x32x16_bf16 v[48:63], v[152:155], v[136:139], v[48:63]
	ds_read_b64_tr_b16 v[202:203], v177 offset:0xca00
	ds_read_b64_tr_b16 v[204:205], v177 offset:0xda00
	s_waitcnt lgkmcnt(6)
	v_mfma_f32_32x32x16_bf16 v[48:63], v[156:159], v[140:143], v[48:63]
	ds_read_b64_tr_b16 v[206:207], v177 offset:0xea00
	ds_read_b64_tr_b16 v[208:209], v177 offset:0xfa00
	s_waitcnt lgkmcnt(6)
	v_mfma_f32_32x32x16_bf16 v[32:47], v[194:197], v[128:131], v[32:47]
	ds_read_b64_tr_b16 v[144:145], v177 offset:0x8c00
	ds_read_b64_tr_b16 v[146:147], v177 offset:0x9c00
	s_waitcnt lgkmcnt(6)
	v_mfma_f32_32x32x16_bf16 v[32:47], v[198:201], v[132:135], v[32:47]
	ds_read_b64_tr_b16 v[148:149], v177 offset:0xac00
	ds_read_b64_tr_b16 v[150:151], v177 offset:0xbc00
	s_waitcnt lgkmcnt(6)
	v_mfma_f32_32x32x16_bf16 v[32:47], v[202:205], v[136:139], v[32:47]
	ds_read_b64_tr_b16 v[152:153], v177 offset:0xcc00
	ds_read_b64_tr_b16 v[154:155], v177 offset:0xdc00
	s_waitcnt lgkmcnt(6)
	v_mfma_f32_32x32x16_bf16 v[32:47], v[206:209], v[140:143], v[32:47]
	ds_read_b64_tr_b16 v[156:157], v177 offset:0xec00
	ds_read_b64_tr_b16 v[158:159], v177 offset:0xfc00
	s_waitcnt lgkmcnt(6)
	v_mfma_f32_32x32x16_bf16 v[16:31], v[144:147], v[128:131], v[16:31]
	ds_read_b64_tr_b16 v[194:195], v177 offset:0x8e00
	ds_read_b64_tr_b16 v[196:197], v177 offset:0x9e00
	s_waitcnt lgkmcnt(6)
	v_mfma_f32_32x32x16_bf16 v[16:31], v[148:151], v[132:135], v[16:31]
	ds_read_b64_tr_b16 v[198:199], v177 offset:0xae00
	ds_read_b64_tr_b16 v[200:201], v177 offset:0xbe00
	s_waitcnt lgkmcnt(6)
	v_mfma_f32_32x32x16_bf16 v[16:31], v[152:155], v[136:139], v[16:31]
	ds_read_b64_tr_b16 v[202:203], v177 offset:0xce00
	ds_read_b64_tr_b16 v[204:205], v177 offset:0xde00
	s_waitcnt lgkmcnt(6)
	v_mfma_f32_32x32x16_bf16 v[16:31], v[156:159], v[140:143], v[16:31]
	ds_read_b64_tr_b16 v[206:207], v177 offset:0xee00
	ds_read_b64_tr_b16 v[208:209], v177 offset:0xfe00
	s_waitcnt lgkmcnt(6)
	v_mfma_f32_32x32x16_bf16 v[0:15], v[194:197], v[128:131], v[0:15]
	ds_read_b128 v[236:239], v181 offset:0
	ds_read_b128 v[240:243], v181 offset:0x2000
	s_waitcnt lgkmcnt(6)
	v_mfma_f32_32x32x16_bf16 v[0:15], v[198:201], v[132:135], v[0:15]
	ds_read_b128 v[244:247], v180 offset:0
	ds_read_b128 v[248:251], v182 offset:0
	s_waitcnt lgkmcnt(6)
	v_mfma_f32_32x32x16_bf16 v[0:15], v[202:205], v[136:139], v[0:15]
	ds_read_b128 v[218:221], v182 offset:0x2000
	ds_read_b128 v[222:225], v180 offset:0x400
	s_waitcnt lgkmcnt(6)
	v_mfma_f32_32x32x16_bf16 v[0:15], v[206:209], v[140:143], v[0:15]
	s_waitcnt lgkmcnt(3)
	s_nop 0
	v_mfma_f32_32x32x16_bf16 v[144:159], v[236:239], v[244:247], 0
	ds_read_b128 v[194:197], v183 offset:0
	ds_read_b128 v[198:201], v183 offset:0x2000
	v_mfma_f32_32x32x16_bf16 v[128:143], v[240:243], v[244:247], 0
	ds_read_b128 v[202:205], v180 offset:0x800
	s_waitcnt lgkmcnt(3)
	v_mfma_f32_32x32x16_bf16 v[144:159], v[248:251], v[222:225], v[144:159]
	ds_read_b128 v[236:239], v184 offset:0
	ds_read_b128 v[240:243], v184 offset:0x2000
	v_mfma_f32_32x32x16_bf16 v[128:143], v[218:221], v[222:225], v[128:143]
	ds_read_b128 v[244:247], v180 offset:0xc00
	s_waitcnt lgkmcnt(3)
	v_mfma_f32_32x32x16_bf16 v[144:159], v[194:197], v[202:205], v[144:159]
	ds_read_b128 v[248:251], v181 offset:0x80
	ds_read_b128 v[218:221], v181 offset:0x2080
	v_mfma_f32_32x32x16_bf16 v[128:143], v[198:201], v[202:205], v[128:143]
	ds_read_b128 v[222:225], v180 offset:0x1000
	s_waitcnt lgkmcnt(3)
	v_mfma_f32_32x32x16_bf16 v[144:159], v[236:239], v[244:247], v[144:159]
	ds_read_b128 v[194:197], v182 offset:0x80
	ds_read_b128 v[198:201], v182 offset:0x2080
	v_mfma_f32_32x32x16_bf16 v[128:143], v[240:243], v[244:247], v[128:143]
	ds_read_b128 v[202:205], v180 offset:0x1400
	s_waitcnt lgkmcnt(3)
	v_mfma_f32_32x32x16_bf16 v[144:159], v[248:251], v[222:225], v[144:159]
	ds_read_b128 v[236:239], v183 offset:0x80
	ds_read_b128 v[240:243], v183 offset:0x2080
	v_mfma_f32_32x32x16_bf16 v[128:143], v[218:221], v[222:225], v[128:143]
	ds_read_b128 v[244:247], v180 offset:0x1800
	s_waitcnt lgkmcnt(3)
	v_mfma_f32_32x32x16_bf16 v[144:159], v[194:197], v[202:205], v[144:159]
	ds_read_b128 v[248:251], v184 offset:0x80
	ds_read_b128 v[218:221], v184 offset:0x2080
	v_mfma_f32_32x32x16_bf16 v[128:143], v[198:201], v[202:205], v[128:143]
	s_waitcnt lgkmcnt(2)
	v_mfma_f32_32x32x16_bf16 v[144:159], v[236:239], v[244:247], v[144:159]
	v_mfma_f32_32x32x16_bf16 v[128:143], v[240:243], v[244:247], v[128:143]
	s_waitcnt lgkmcnt(0)
	v_mfma_f32_32x32x16_bf16 v[144:159], v[248:251], v[166:169], v[144:159]
	v_mfma_f32_32x32x16_bf16 v[128:143], v[218:221], v[166:169], v[128:143]
	s_bitcmp0_b32 s100, 8
	s_cbranch_scc1 .Lstg_a11
	s_waitcnt vmcnt(0)
	s_waitcnt lgkmcnt(0)
	s_barrier

.LBB0_589:
	ds_read_b64_tr_b16 v[144:145], v177 offset:0
	ds_read_b64_tr_b16 v[146:147], v177 offset:0x1000
	ds_read_b64_tr_b16 v[148:149], v177 offset:0x2000
	ds_read_b64_tr_b16 v[150:151], v177 offset:0x3000
	ds_read_b64_tr_b16 v[152:153], v177 offset:0x4000
	ds_read_b64_tr_b16 v[154:155], v177 offset:0x5000
	ds_read_b64_tr_b16 v[156:157], v177 offset:0x6000
	ds_read_b64_tr_b16 v[158:159], v177 offset:0x7000
	s_waitcnt lgkmcnt(6)
	s_nop 0
	v_mfma_f32_32x32x16_bf16 v[112:127], v[144:147], v[128:131], v[112:127]
	ds_read_b64_tr_b16 v[192:193], v177 offset:0x200
	ds_read_b64_tr_b16 v[194:195], v177 offset:0x1200
	s_waitcnt lgkmcnt(6)
	v_mfma_f32_32x32x16_bf16 v[112:127], v[148:151], v[132:135], v[112:127]
	ds_read_b64_tr_b16 v[196:197], v177 offset:0x2200
	ds_read_b64_tr_b16 v[198:199], v177 offset:0x3200
	s_waitcnt lgkmcnt(6)
	v_mfma_f32_32x32x16_bf16 v[112:127], v[152:155], v[136:139], v[112:127]
	ds_read_b64_tr_b16 v[200:201], v177 offset:0x4200
	ds_read_b64_tr_b16 v[202:203], v177 offset:0x5200
	s_waitcnt lgkmcnt(6)
	v_mfma_f32_32x32x16_bf16 v[112:127], v[156:159], v[140:143], v[112:127]
	ds_read_b64_tr_b16 v[204:205], v177 offset:0x6200
	ds_read_b64_tr_b16 v[206:207], v177 offset:0x7200
	s_waitcnt lgkmcnt(6)
	v_mfma_f32_32x32x16_bf16 v[96:111], v[192:195], v[128:131], v[96:111]
	ds_read_b64_tr_b16 v[144:145], v177 offset:0x400
	ds_read_b64_tr_b16 v[146:147], v177 offset:0x1400
	s_waitcnt lgkmcnt(6)
	v_mfma_f32_32x32x16_bf16 v[96:111], v[196:199], v[132:135], v[96:111]
	ds_read_b64_tr_b16 v[148:149], v177 offset:0x2400
	ds_read_b64_tr_b16 v[150:151], v177 offset:0x3400
	s_waitcnt lgkmcnt(6)
	v_mfma_f32_32x32x16_bf16 v[96:111], v[200:203], v[136:139], v[96:111]
	ds_read_b64_tr_b16 v[152:153], v177 offset:0x4400
	ds_read_b64_tr_b16 v[154:155], v177 offset:0x5400
	s_waitcnt lgkmcnt(6)
	v_mfma_f32_32x32x16_bf16 v[96:111], v[204:207], v[140:143], v[96:111]
	ds_read_b64_tr_b16 v[156:157], v177 offset:0x6400
	ds_read_b64_tr_b16 v[158:159], v177 offset:0x7400
	s_waitcnt lgkmcnt(6)
	v_mfma_f32_32x32x16_bf16 v[80:95], v[144:147], v[128:131], v[80:95]
	ds_read_b64_tr_b16 v[192:193], v177 offset:0x600
	ds_read_b64_tr_b16 v[194:195], v177 offset:0x1600
	s_waitcnt lgkmcnt(6)
	v_mfma_f32_32x32x16_bf16 v[80:95], v[148:151], v[132:135], v[80:95]
	ds_read_b64_tr_b16 v[196:197], v177 offset:0x2600
	ds_read_b64_tr_b16 v[198:199], v177 offset:0x3600
	s_waitcnt lgkmcnt(6)
	v_mfma_f32_32x32x16_bf16 v[80:95], v[152:155], v[136:139], v[80:95]
	ds_read_b64_tr_b16 v[200:201], v177 offset:0x4600
	ds_read_b64_tr_b16 v[202:203], v177 offset:0x5600
	s_waitcnt lgkmcnt(6)
	v_mfma_f32_32x32x16_bf16 v[80:95], v[156:159], v[140:143], v[80:95]
	ds_read_b64_tr_b16 v[204:205], v177 offset:0x6600
	ds_read_b64_tr_b16 v[206:207], v177 offset:0x7600
	s_waitcnt lgkmcnt(6)
	v_mfma_f32_32x32x16_bf16 v[64:79], v[192:195], v[128:131], v[64:79]
	ds_read_b64_tr_b16 v[144:145], v177 offset:0x800
	ds_read_b64_tr_b16 v[146:147], v177 offset:0x1800
	s_waitcnt lgkmcnt(6)
	v_mfma_f32_32x32x16_bf16 v[64:79], v[196:199], v[132:135], v[64:79]
	ds_read_b64_tr_b16 v[148:149], v177 offset:0x2800
	ds_read_b64_tr_b16 v[150:151], v177 offset:0x3800
	s_waitcnt lgkmcnt(6)
	v_mfma_f32_32x32x16_bf16 v[64:79], v[200:203], v[136:139], v[64:79]
	ds_read_b64_tr_b16 v[152:153], v177 offset:0x4800
	ds_read_b64_tr_b16 v[154:155], v177 offset:0x5800
	s_waitcnt lgkmcnt(6)
	v_mfma_f32_32x32x16_bf16 v[64:79], v[204:207], v[140:143], v[64:79]
	ds_read_b64_tr_b16 v[156:157], v177 offset:0x6800
	ds_read_b64_tr_b16 v[158:159], v177 offset:0x7800
	s_waitcnt lgkmcnt(6)
	v_mfma_f32_32x32x16_bf16 v[48:63], v[144:147], v[128:131], v[48:63]
	ds_read_b64_tr_b16 v[192:193], v177 offset:0xa00
	ds_read_b64_tr_b16 v[194:195], v177 offset:0x1a00
	s_waitcnt lgkmcnt(6)
	v_mfma_f32_32x32x16_bf16 v[48:63], v[148:151], v[132:135], v[48:63]
	ds_read_b64_tr_b16 v[196:197], v177 offset:0x2a00
	ds_read_b64_tr_b16 v[198:199], v177 offset:0x3a00
	s_waitcnt lgkmcnt(6)
	v_mfma_f32_32x32x16_bf16 v[48:63], v[152:155], v[136:139], v[48:63]
	ds_read_b64_tr_b16 v[200:201], v177 offset:0x4a00
	ds_read_b64_tr_b16 v[202:203], v177 offset:0x5a00
	s_waitcnt lgkmcnt(6)
	v_mfma_f32_32x32x16_bf16 v[48:63], v[156:159], v[140:143], v[48:63]
	ds_read_b64_tr_b16 v[204:205], v177 offset:0x6a00
	ds_read_b64_tr_b16 v[206:207], v177 offset:0x7a00
	s_waitcnt lgkmcnt(6)
	v_mfma_f32_32x32x16_bf16 v[32:47], v[192:195], v[128:131], v[32:47]
	ds_read_b64_tr_b16 v[144:145], v177 offset:0xc00
	ds_read_b64_tr_b16 v[146:147], v177 offset:0x1c00
	s_waitcnt lgkmcnt(6)
	v_mfma_f32_32x32x16_bf16 v[32:47], v[196:199], v[132:135], v[32:47]
	ds_read_b64_tr_b16 v[148:149], v177 offset:0x2c00
	ds_read_b64_tr_b16 v[150:151], v177 offset:0x3c00
	s_waitcnt lgkmcnt(6)
	v_mfma_f32_32x32x16_bf16 v[32:47], v[200:203], v[136:139], v[32:47]
	ds_read_b64_tr_b16 v[152:153], v177 offset:0x4c00
	ds_read_b64_tr_b16 v[154:155], v177 offset:0x5c00
	s_waitcnt lgkmcnt(6)
	v_mfma_f32_32x32x16_bf16 v[32:47], v[204:207], v[140:143], v[32:47]
	ds_read_b64_tr_b16 v[156:157], v177 offset:0x6c00
	ds_read_b64_tr_b16 v[158:159], v177 offset:0x7c00
	s_waitcnt lgkmcnt(6)
	v_mfma_f32_32x32x16_bf16 v[16:31], v[144:147], v[128:131], v[16:31]
	ds_read_b64_tr_b16 v[192:193], v177 offset:0xe00
	ds_read_b64_tr_b16 v[194:195], v177 offset:0x1e00
	s_waitcnt lgkmcnt(6)
	v_mfma_f32_32x32x16_bf16 v[16:31], v[148:151], v[132:135], v[16:31]
	ds_read_b64_tr_b16 v[196:197], v177 offset:0x2e00
	ds_read_b64_tr_b16 v[198:199], v177 offset:0x3e00
	s_waitcnt lgkmcnt(6)
	v_mfma_f32_32x32x16_bf16 v[16:31], v[152:155], v[136:139], v[16:31]
	ds_read_b64_tr_b16 v[200:201], v177 offset:0x4e00
	ds_read_b64_tr_b16 v[202:203], v177 offset:0x5e00
	s_waitcnt lgkmcnt(6)
	v_mfma_f32_32x32x16_bf16 v[16:31], v[156:159], v[140:143], v[16:31]
	ds_read_b64_tr_b16 v[204:205], v177 offset:0x6e00
	ds_read_b64_tr_b16 v[206:207], v177 offset:0x7e00
	s_waitcnt lgkmcnt(6)
	v_mfma_f32_32x32x16_bf16 v[0:15], v[192:195], v[128:131], v[0:15]
	ds_read_b128 v[236:239], v188 offset:0
	ds_read_b128 v[240:243], v188 offset:0x2000
	s_waitcnt lgkmcnt(6)
	v_mfma_f32_32x32x16_bf16 v[0:15], v[196:199], v[132:135], v[0:15]
	ds_read_b128 v[244:247], v180 offset:0
	ds_read_b128 v[248:251], v187 offset:0
	s_waitcnt lgkmcnt(6)
	v_mfma_f32_32x32x16_bf16 v[0:15], v[200:203], v[136:139], v[0:15]
	ds_read_b128 v[218:221], v187 offset:0x2000
	ds_read_b128 v[222:225], v180 offset:0x400
	s_waitcnt lgkmcnt(6)
	v_mfma_f32_32x32x16_bf16 v[0:15], v[204:207], v[140:143], v[0:15]
	s_waitcnt lgkmcnt(3)
	s_nop 0
	v_mfma_f32_32x32x16_bf16 v[144:159], v[236:239], v[244:247], 0
	ds_read_b128 v[192:195], v186 offset:0
	ds_read_b128 v[196:199], v186 offset:0x2000
	v_mfma_f32_32x32x16_bf16 v[128:143], v[240:243], v[244:247], 0
	ds_read_b128 v[200:203], v180 offset:0x800
	s_waitcnt lgkmcnt(3)
	v_mfma_f32_32x32x16_bf16 v[144:159], v[248:251], v[222:225], v[144:159]
	ds_read_b128 v[236:239], v185 offset:0
	ds_read_b128 v[240:243], v185 offset:0x2000
	v_mfma_f32_32x32x16_bf16 v[128:143], v[218:221], v[222:225], v[128:143]
	ds_read_b128 v[244:247], v180 offset:0xc00
	s_waitcnt lgkmcnt(3)
	v_mfma_f32_32x32x16_bf16 v[144:159], v[192:195], v[200:203], v[144:159]
	ds_read_b128 v[248:251], v188 offset:0x80
	ds_read_b128 v[218:221], v188 offset:0x2080
	v_mfma_f32_32x32x16_bf16 v[128:143], v[196:199], v[200:203], v[128:143]
	ds_read_b128 v[222:225], v180 offset:0x1000
	s_waitcnt lgkmcnt(3)
	v_mfma_f32_32x32x16_bf16 v[144:159], v[236:239], v[244:247], v[144:159]
	ds_read_b128 v[192:195], v187 offset:0x80
	ds_read_b128 v[196:199], v187 offset:0x2080
	v_mfma_f32_32x32x16_bf16 v[128:143], v[240:243], v[244:247], v[128:143]
	ds_read_b128 v[200:203], v180 offset:0x1400
	s_waitcnt lgkmcnt(3)
	v_mfma_f32_32x32x16_bf16 v[144:159], v[248:251], v[222:225], v[144:159]
	ds_read_b128 v[236:239], v186 offset:0x80
	ds_read_b128 v[240:243], v186 offset:0x2080
	v_mfma_f32_32x32x16_bf16 v[128:143], v[218:221], v[222:225], v[128:143]
	ds_read_b128 v[244:247], v180 offset:0x1800
	s_waitcnt lgkmcnt(3)
	v_mfma_f32_32x32x16_bf16 v[144:159], v[192:195], v[200:203], v[144:159]
	ds_read_b128 v[248:251], v185 offset:0x80
	ds_read_b128 v[218:221], v185 offset:0x2080
	v_mfma_f32_32x32x16_bf16 v[128:143], v[196:199], v[200:203], v[128:143]
	s_waitcnt lgkmcnt(2)
	v_mfma_f32_32x32x16_bf16 v[144:159], v[236:239], v[244:247], v[144:159]
	v_mfma_f32_32x32x16_bf16 v[128:143], v[240:243], v[244:247], v[128:143]
	s_waitcnt lgkmcnt(0)
	v_mfma_f32_32x32x16_bf16 v[144:159], v[248:251], v[166:169], v[144:159]
	v_mfma_f32_32x32x16_bf16 v[128:143], v[218:221], v[166:169], v[128:143]
	s_bitcmp0_b32 s100, 8
	s_cbranch_scc1 .Lstg_a18
	s_waitcnt vmcnt(0)
	s_waitcnt lgkmcnt(0)
	s_barrier

.LBB0_597:
	ds_read_b64_tr_b16 v[144:145], v177 offset:0x8000
	ds_read_b64_tr_b16 v[146:147], v177 offset:0x9000
	ds_read_b64_tr_b16 v[148:149], v177 offset:0xa000
	ds_read_b64_tr_b16 v[150:151], v177 offset:0xb000
	ds_read_b64_tr_b16 v[152:153], v177 offset:0xc000
	ds_read_b64_tr_b16 v[154:155], v177 offset:0xd000
	ds_read_b64_tr_b16 v[156:157], v177 offset:0xe000
	ds_read_b64_tr_b16 v[158:159], v177 offset:0xf000
	s_waitcnt lgkmcnt(6)
	s_nop 0
	v_mfma_f32_32x32x16_bf16 v[112:127], v[144:147], v[128:131], v[112:127]
	ds_read_b64_tr_b16 v[194:195], v177 offset:0x8200
	ds_read_b64_tr_b16 v[196:197], v177 offset:0x9200
	s_waitcnt lgkmcnt(6)
	v_mfma_f32_32x32x16_bf16 v[112:127], v[148:151], v[132:135], v[112:127]
	ds_read_b64_tr_b16 v[198:199], v177 offset:0xa200
	ds_read_b64_tr_b16 v[200:201], v177 offset:0xb200
	s_waitcnt lgkmcnt(6)
	v_mfma_f32_32x32x16_bf16 v[112:127], v[152:155], v[136:139], v[112:127]
	ds_read_b64_tr_b16 v[202:203], v177 offset:0xc200
	ds_read_b64_tr_b16 v[204:205], v177 offset:0xd200
	s_waitcnt lgkmcnt(6)
	v_mfma_f32_32x32x16_bf16 v[112:127], v[156:159], v[140:143], v[112:127]
	ds_read_b64_tr_b16 v[206:207], v177 offset:0xe200
	ds_read_b64_tr_b16 v[208:209], v177 offset:0xf200
	s_waitcnt lgkmcnt(6)
	v_mfma_f32_32x32x16_bf16 v[96:111], v[194:197], v[128:131], v[96:111]
	ds_read_b64_tr_b16 v[144:145], v177 offset:0x8400
	ds_read_b64_tr_b16 v[146:147], v177 offset:0x9400
	s_waitcnt lgkmcnt(6)
	v_mfma_f32_32x32x16_bf16 v[96:111], v[198:201], v[132:135], v[96:111]
	ds_read_b64_tr_b16 v[148:149], v177 offset:0xa400
	ds_read_b64_tr_b16 v[150:151], v177 offset:0xb400
	s_waitcnt lgkmcnt(6)
	v_mfma_f32_32x32x16_bf16 v[96:111], v[202:205], v[136:139], v[96:111]
	ds_read_b64_tr_b16 v[152:153], v177 offset:0xc400
	ds_read_b64_tr_b16 v[154:155], v177 offset:0xd400
	s_waitcnt lgkmcnt(6)
	v_mfma_f32_32x32x16_bf16 v[96:111], v[206:209], v[140:143], v[96:111]
	ds_read_b64_tr_b16 v[156:157], v177 offset:0xe400
	ds_read_b64_tr_b16 v[158:159], v177 offset:0xf400
	s_waitcnt lgkmcnt(6)
	v_mfma_f32_32x32x16_bf16 v[80:95], v[144:147], v[128:131], v[80:95]
	ds_read_b64_tr_b16 v[194:195], v177 offset:0x8600
	ds_read_b64_tr_b16 v[196:197], v177 offset:0x9600
	s_waitcnt lgkmcnt(6)
	v_mfma_f32_32x32x16_bf16 v[80:95], v[148:151], v[132:135], v[80:95]
	ds_read_b64_tr_b16 v[198:199], v177 offset:0xa600
	ds_read_b64_tr_b16 v[200:201], v177 offset:0xb600
	s_waitcnt lgkmcnt(6)
	v_mfma_f32_32x32x16_bf16 v[80:95], v[152:155], v[136:139], v[80:95]
	ds_read_b64_tr_b16 v[202:203], v177 offset:0xc600
	ds_read_b64_tr_b16 v[204:205], v177 offset:0xd600
	s_waitcnt lgkmcnt(6)
	v_mfma_f32_32x32x16_bf16 v[80:95], v[156:159], v[140:143], v[80:95]
	ds_read_b64_tr_b16 v[206:207], v177 offset:0xe600
	ds_read_b64_tr_b16 v[208:209], v177 offset:0xf600
	s_waitcnt lgkmcnt(6)
	v_mfma_f32_32x32x16_bf16 v[64:79], v[194:197], v[128:131], v[64:79]
	ds_read_b64_tr_b16 v[144:145], v177 offset:0x8800
	ds_read_b64_tr_b16 v[146:147], v177 offset:0x9800
	s_waitcnt lgkmcnt(6)
	v_mfma_f32_32x32x16_bf16 v[64:79], v[198:201], v[132:135], v[64:79]
	ds_read_b64_tr_b16 v[148:149], v177 offset:0xa800
	ds_read_b64_tr_b16 v[150:151], v177 offset:0xb800
	s_waitcnt lgkmcnt(6)
	v_mfma_f32_32x32x16_bf16 v[64:79], v[202:205], v[136:139], v[64:79]
	ds_read_b64_tr_b16 v[152:153], v177 offset:0xc800
	ds_read_b64_tr_b16 v[154:155], v177 offset:0xd800
	s_waitcnt lgkmcnt(6)
	v_mfma_f32_32x32x16_bf16 v[64:79], v[206:209], v[140:143], v[64:79]
	ds_read_b64_tr_b16 v[156:157], v177 offset:0xe800
	ds_read_b64_tr_b16 v[158:159], v177 offset:0xf800
	s_waitcnt lgkmcnt(6)
	v_mfma_f32_32x32x16_bf16 v[48:63], v[144:147], v[128:131], v[48:63]
	ds_read_b64_tr_b16 v[194:195], v177 offset:0x8a00
	ds_read_b64_tr_b16 v[196:197], v177 offset:0x9a00
	s_waitcnt lgkmcnt(6)
	v_mfma_f32_32x32x16_bf16 v[48:63], v[148:151], v[132:135], v[48:63]
	ds_read_b64_tr_b16 v[198:199], v177 offset:0xaa00
	ds_read_b64_tr_b16 v[200:201], v177 offset:0xba00
	s_waitcnt lgkmcnt(6)
	v_mfma_f32_32x32x16_bf16 v[48:63], v[152:155], v[136:139], v[48:63]
	ds_read_b64_tr_b16 v[202:203], v177 offset:0xca00
	ds_read_b64_tr_b16 v[204:205], v177 offset:0xda00
	s_waitcnt lgkmcnt(6)
	v_mfma_f32_32x32x16_bf16 v[48:63], v[156:159], v[140:143], v[48:63]
	ds_read_b64_tr_b16 v[206:207], v177 offset:0xea00
	ds_read_b64_tr_b16 v[208:209], v177 offset:0xfa00
	s_waitcnt lgkmcnt(6)
	v_mfma_f32_32x32x16_bf16 v[32:47], v[194:197], v[128:131], v[32:47]
	ds_read_b64_tr_b16 v[144:145], v177 offset:0x8c00
	ds_read_b64_tr_b16 v[146:147], v177 offset:0x9c00
	s_waitcnt lgkmcnt(6)
	v_mfma_f32_32x32x16_bf16 v[32:47], v[198:201], v[132:135], v[32:47]
	ds_read_b64_tr_b16 v[148:149], v177 offset:0xac00
	ds_read_b64_tr_b16 v[150:151], v177 offset:0xbc00
	s_waitcnt lgkmcnt(6)
	v_mfma_f32_32x32x16_bf16 v[32:47], v[202:205], v[136:139], v[32:47]
	ds_read_b64_tr_b16 v[152:153], v177 offset:0xcc00
	ds_read_b64_tr_b16 v[154:155], v177 offset:0xdc00
	s_waitcnt lgkmcnt(6)
	v_mfma_f32_32x32x16_bf16 v[32:47], v[206:209], v[140:143], v[32:47]
	ds_read_b64_tr_b16 v[156:157], v177 offset:0xec00
	ds_read_b64_tr_b16 v[158:159], v177 offset:0xfc00
	s_waitcnt lgkmcnt(6)
	v_mfma_f32_32x32x16_bf16 v[16:31], v[144:147], v[128:131], v[16:31]
	ds_read_b64_tr_b16 v[194:195], v177 offset:0x8e00
	ds_read_b64_tr_b16 v[196:197], v177 offset:0x9e00
	s_waitcnt lgkmcnt(6)
	v_mfma_f32_32x32x16_bf16 v[16:31], v[148:151], v[132:135], v[16:31]
	ds_read_b64_tr_b16 v[198:199], v177 offset:0xae00
	ds_read_b64_tr_b16 v[200:201], v177 offset:0xbe00
	s_waitcnt lgkmcnt(6)
	v_mfma_f32_32x32x16_bf16 v[16:31], v[152:155], v[136:139], v[16:31]
	ds_read_b64_tr_b16 v[202:203], v177 offset:0xce00
	ds_read_b64_tr_b16 v[204:205], v177 offset:0xde00
	s_waitcnt lgkmcnt(6)
	v_mfma_f32_32x32x16_bf16 v[16:31], v[156:159], v[140:143], v[16:31]
	ds_read_b64_tr_b16 v[206:207], v177 offset:0xee00
	ds_read_b64_tr_b16 v[208:209], v177 offset:0xfe00
	s_waitcnt lgkmcnt(6)
	v_mfma_f32_32x32x16_bf16 v[0:15], v[194:197], v[128:131], v[0:15]
	ds_read_b128 v[236:239], v181 offset:0
	ds_read_b128 v[240:243], v181 offset:0x2000
	s_waitcnt lgkmcnt(6)
	v_mfma_f32_32x32x16_bf16 v[0:15], v[198:201], v[132:135], v[0:15]
	ds_read_b128 v[244:247], v180 offset:0
	ds_read_b128 v[248:251], v182 offset:0
	s_waitcnt lgkmcnt(6)
	v_mfma_f32_32x32x16_bf16 v[0:15], v[202:205], v[136:139], v[0:15]
	ds_read_b128 v[218:221], v182 offset:0x2000
	ds_read_b128 v[222:225], v180 offset:0x400
	s_waitcnt lgkmcnt(6)
	v_mfma_f32_32x32x16_bf16 v[0:15], v[206:209], v[140:143], v[0:15]
	s_waitcnt lgkmcnt(3)
	s_nop 0
	v_mfma_f32_32x32x16_bf16 v[144:159], v[236:239], v[244:247], 0
	ds_read_b128 v[194:197], v183 offset:0
	ds_read_b128 v[198:201], v183 offset:0x2000
	v_mfma_f32_32x32x16_bf16 v[128:143], v[240:243], v[244:247], 0
	ds_read_b128 v[202:205], v180 offset:0x800
	s_waitcnt lgkmcnt(3)
	v_mfma_f32_32x32x16_bf16 v[144:159], v[248:251], v[222:225], v[144:159]
	ds_read_b128 v[236:239], v184 offset:0
	ds_read_b128 v[240:243], v184 offset:0x2000
	v_mfma_f32_32x32x16_bf16 v[128:143], v[218:221], v[222:225], v[128:143]
	ds_read_b128 v[244:247], v180 offset:0xc00
	s_waitcnt lgkmcnt(3)
	v_mfma_f32_32x32x16_bf16 v[144:159], v[194:197], v[202:205], v[144:159]
	ds_read_b128 v[248:251], v181 offset:0x80
	ds_read_b128 v[218:221], v181 offset:0x2080
	v_mfma_f32_32x32x16_bf16 v[128:143], v[198:201], v[202:205], v[128:143]
	ds_read_b128 v[222:225], v180 offset:0x1000
	s_waitcnt lgkmcnt(3)
	v_mfma_f32_32x32x16_bf16 v[144:159], v[236:239], v[244:247], v[144:159]
	ds_read_b128 v[194:197], v182 offset:0x80
	ds_read_b128 v[198:201], v182 offset:0x2080
	v_mfma_f32_32x32x16_bf16 v[128:143], v[240:243], v[244:247], v[128:143]
	ds_read_b128 v[202:205], v180 offset:0x1400
	s_waitcnt lgkmcnt(3)
	v_mfma_f32_32x32x16_bf16 v[144:159], v[248:251], v[222:225], v[144:159]
	ds_read_b128 v[236:239], v183 offset:0x80
	ds_read_b128 v[240:243], v183 offset:0x2080
	v_mfma_f32_32x32x16_bf16 v[128:143], v[218:221], v[222:225], v[128:143]
	ds_read_b128 v[244:247], v180 offset:0x1800
	s_waitcnt lgkmcnt(3)
	v_mfma_f32_32x32x16_bf16 v[144:159], v[194:197], v[202:205], v[144:159]
	ds_read_b128 v[248:251], v184 offset:0x80
	ds_read_b128 v[218:221], v184 offset:0x2080
	v_mfma_f32_32x32x16_bf16 v[128:143], v[198:201], v[202:205], v[128:143]
	s_waitcnt lgkmcnt(2)
	v_mfma_f32_32x32x16_bf16 v[144:159], v[236:239], v[244:247], v[144:159]
	v_mfma_f32_32x32x16_bf16 v[128:143], v[240:243], v[244:247], v[128:143]
	s_waitcnt lgkmcnt(0)
	v_mfma_f32_32x32x16_bf16 v[144:159], v[248:251], v[166:169], v[144:159]
	v_mfma_f32_32x32x16_bf16 v[128:143], v[218:221], v[166:169], v[128:143]
	s_bitcmp0_b32 s100, 8
	s_cbranch_scc1 .Lstg_a19
	s_waitcnt vmcnt(0)
	s_waitcnt lgkmcnt(0)
	s_barrier
